# removes the conversion point at the NA tail (GLA finishes before the NA queue is exhausted, so it only added a flag round trip)
# baseline (speedup 1.0000x reference)
; #define LAS __attribute__((address_space(3)))
; __global__ void __launch_bounds__(512, 2) mk_fwd(Args a) {
;     ...
;         if (bid < 64) { gla_fast_unit(bid, Pb, a.in[I_GLAWUP], a.in[I_GLABUP], Of, Ob, lds); }
;         unsigned* qctr = (unsigned*)(ws + WS_CTL) + 8192 + 64 * rep;
;         for (;;) {
;             __syncthreads();
;             if (tid == 0) *(volatile LAS unsigned*)(lds + LDS_BARW + 32) = atomicAdd(qctr, 1u);
;             __syncthreads();
;             const unsigned u = *(volatile LAS unsigned*)(lds + LDS_BARW + 32);
;             if (u >= (unsigned)(NB * 8 * 64)) break;
;             na_fast_unit((int)u, Pb, a.in[I_RPB], AO, lds);
.LBB0_1205:
	s_waitcnt lgkmcnt(0)
	s_barrier
.LBB0_1206:
	v_or_b32_e32 v3, 0x600, v0
	s_add_u32 s8, s94, 0x8000
	v_and_b32_e32 v2, 0x78, v181
	v_or_b32_e32 v104, 64, v168
	v_lshrrev_b32_e32 v105, 4, v3
	v_readlane_b32 s6, v255, 3
	s_addc_u32 s9, s95, 0
	v_bfe_u32 v106, v3, 4, 6
	v_mul_u32_u24_e32 v107, 0x110, v168
	v_mul_u32_u24_e32 v108, 0x110, v170
	v_mul_u32_u24_e32 v109, 0x120, v104
	v_mul_u32_u24_e32 v110, 0x110, v105
	v_mul_u32_u24_e32 v111, 0x120, v105
	s_add_i32 s2, 0, 0x11800
	s_add_i32 s3, 0, 0x1a000
	v_lshlrev_b32_e32 v114, 11, v86
	v_lshl_add_u32 v115, v1, 2, 0
	v_lshlrev_b32_e32 v86, 1, v1
	v_readlane_b32 s7, v255, 4
	v_mov_b32_e32 v3, 0x200
	s_add_i32 s45, 0, 0x23fe0
	v_lshlrev_b32_e32 v92, 1, v2
	v_mbcnt_lo_u32_b32 v2, -1, 0
	v_cmp_eq_u32_e64 s[4:5], 0, v0
	s_movk_i32 s13, 0x110
	v_add_u32_e32 v112, s2, v176
	v_add_u32_e32 v113, s3, v178
	v_add_u32_e32 v116, v115, v114
	v_lshl_add_u64 v[88:89], s[6:7], 0, v[86:87]
	v_lshl_or_b32 v117, v169, 9, v3
	v_lshlrev_b32_e32 v118, 9, v180
	v_lshlrev_b32_e32 v119, 9, v179
	v_add_u32_e32 v120, 0, v176
	v_add_u32_e32 v121, 0, v178
	v_add_u32_e32 v122, s2, v177
	v_add_u32_e32 v123, s3, v177
	v_lshl_add_u32 v124, v169, 2, 0
	v_mov_b32_e32 v125, s45
	s_movk_i32 s46, 0x3200
	s_mov_b64 s[10:11], 0x1400
	s_movk_i32 s47, 0x1000
	v_add_u32_e32 v126, v174, v107
	v_add_u32_e32 v127, v174, v171
	v_add_u32_e32 v128, v174, v108
	v_add_u32_e32 v129, v174, v172
	v_add_u32_e32 v130, v174, v109
	v_add_u32_e32 v131, v174, v110
	v_add_u32_e32 v132, v174, v111
	s_mov_b32 s12, 0x3db504f3
	v_lshlrev_b32_e32 v90, 1, v175
	v_mbcnt_hi_u32_b32 v133, -1, v2
	s_and_saveexec_b64 s[2:3], s[4:5]
	v_mov_b32_e32 v3, 1
	global_atomic_add v253, v87, v3, s[8:9] sc0
	s_waitcnt vmcnt(0)
	s_mov_b64 exec, s[2:3]
	s_branch .LBB0_1209
